# q up-projection epilogue: the 12 norm-weight loads requested together with the statistics loads (free VGPRs), counted waits instead of three dependent load groups
# baseline (speedup 1.0000x reference)
; #define MFMA(a, b, c) __builtin_amdgcn_mfma_f32_32x32x16_bf16((a), (b), (c), 0, 0, 0)
; DEV float fast_rsq(float x) { return __builtin_amdgcn_rsqf(x); }
; DEV float half_sum(float v) { float a, b; swap32(v, a, b); return a + b; }
; DEV void tok_info(int tok, int& b, int& kidx) { if (tok < NLAT) { b = tok >> 14; kidx = tok & 16383; } else { const int j = tok - NLAT; b = j >> 8; kidx = 16384 + (j & 255); } }
;     ...
;         for (int ks = 0; ks < 4; ++ks) {
;             bf16x8 af[TM], wf[TN];
; #pragma unroll
;             for (int a = 0; a < TM; ++a) af[a] = lds_b128(sb + arow + a * 4096 + koff[ks]);
; #pragma unroll
;             for (int b = 0; b < TN; ++b) wf[b] = lds_b128(sb + brow + b * 4096 + koff[ks]);
; #pragma unroll
;             for (int a = 0; a < TM; ++a)
; #pragma unroll
;                 for (int b = 0; b < TN; ++b) acc[a][b] = F16 ? __builtin_amdgcn_mfma_f32_32x32x16_f16(__builtin_bit_cast(f16x8, wf[b]), __builtin_bit_cast(f16x8, af[a]), acc[a][b], 0, 0, 0)
;                                                             : MFMA(wf[b], af[a], acc[a][b]);
;         } }
;     template <int TM, int TN> DEV void run(const f32x16 (&acc)[TM][TN], int mw, int cb, int r, int h) const {
;     ...
;         for (int tm = 0; tm < TM; ++tm) {
;             const int tok = mw + tm * 32 + r; int b, kidx; tok_info(tok, b, kidx);
;             const float* ssp = (const float*)(ws + WS_SS) + (size_t)tok * 16;
;             const float rq = fast_rsq((ssp[0] + ssp[1] + ssp[2] + ssp[3] + ssp[4] + ssp[5]) * (1.0f / 384.0f) + EPS);
;             const float s1 = half_sum(sumsq16(acc[tm][0]) + sumsq16(acc[tm][1])) * rq * rq;
;             const float s2 = half_sum(sumsq16(acc[tm][2])) * rq * rq;
;             const float r1 = fast_rsq(s1 * (1.0f / 64.0f) + EPS) * rq, r2 = fast_rsq(s2 * (1.0f / 32.0f) + EPS) * rq;
;             unsigned char* dst = ws + WS_QC + (size_t)tok * 768 + hd * 128 + 16 * h;
; #pragma unroll
;             for (int tn = 0; tn < 3; ++tn) { f32x16 v; const float rr = (tn < 2 ? r1 : r2);
; #pragma unroll
;                 for (int i = 0; i < 16; ++i) v[i] = acc[tm][tn][i] * rr * gain[tn * 32 + 16 * h + i];
.LBB0_585:
	v_and_b32_e32 v58, 0xffffffe0, v68
	ds_read_b128 v[50:53], v91
	ds_read_b128 v[54:57], v90 offset:16384
	ds_read_b128 v[64:67], v90 offset:20480
	ds_read_b128 v[68:71], v90 offset:24576
	s_mov_b32 s2, 0x8000
	s_waitcnt lgkmcnt(0)
	v_mfma_f32_32x32x16_bf16 v[34:49], v[54:57], v[50:53], v[34:49]
	v_lshlrev_b32_e32 v178, 4, v60
	v_mfma_f32_32x32x16_bf16 v[18:33], v[64:67], v[50:53], v[18:33]
	v_mfma_f32_32x32x16_bf16 v[2:17], v[68:71], v[50:53], v[2:17]
	ds_read_b128 v[50:53], v89
	ds_read_b128 v[54:57], v88 offset:16384
	ds_read_b128 v[64:67], v88 offset:20480
	ds_read_b128 v[68:71], v88 offset:24576
	s_waitcnt lgkmcnt(0)
	v_mfma_f32_32x32x16_bf16 v[34:49], v[54:57], v[50:53], v[34:49]
	v_mfma_f32_32x32x16_bf16 v[18:33], v[64:67], v[50:53], v[18:33]
	v_mfma_f32_32x32x16_bf16 v[2:17], v[68:71], v[50:53], v[2:17]
	ds_read_b128 v[50:53], v87
	ds_read_b128 v[54:57], v85 offset:16384
	ds_read_b128 v[64:67], v85 offset:20480
	ds_read_b128 v[68:71], v85 offset:24576
	s_waitcnt lgkmcnt(0)
	v_mfma_f32_32x32x16_bf16 v[34:49], v[54:57], v[50:53], v[34:49]
	v_mfma_f32_32x32x16_bf16 v[18:33], v[64:67], v[50:53], v[18:33]
	v_mfma_f32_32x32x16_bf16 v[2:17], v[68:71], v[50:53], v[2:17]
	ds_read_b128 v[50:53], v86
	ds_read_b128 v[54:57], v84 offset:16384
	ds_read_b128 v[64:67], v84 offset:20480
	ds_read_b128 v[68:71], v84 offset:24576
	s_waitcnt lgkmcnt(0)
	s_barrier
	s_waitcnt lgkmcnt(0)
	v_mfma_f32_32x32x16_bf16 v[34:49], v[54:57], v[50:53], v[34:49]
	v_mfma_f32_32x32x16_bf16 v[18:33], v[64:67], v[50:53], v[18:33]
	v_mfma_f32_32x32x16_bf16 v[2:17], v[68:71], v[50:53], v[2:17]
	v_add_u32_e32 v50, s28, v62
	v_mul_i32_i24_e32 v50, 0x2aab, v50
	v_lshrrev_b32_e32 v51, 31, v50
	v_ashrrev_i32_e32 v50, 20, v50
	v_add_u16_e32 v56, v50, v51
	v_or_b32_e32 v50, s19, v61
	v_add_u32_e32 v52, v58, v50
	v_ashrrev_i32_e32 v53, 31, v52
	v_lshlrev_b64 v[50:51], 6, v[52:53]
	v_cmp_gt_i32_e32 vcc, s2, v52
	v_lshl_add_u64 v[54:55], s[58:59], 0, v[50:51]
	v_mov_b64_e32 v[50:51], s[60:61]
	s_movk_i32 s2, 0x300
	v_lshlrev_b32_sdwa v56, v249, sext(v56) dst_sel:DWORD dst_unused:UNUSED_PAD src0_sel:DWORD src1_sel:WORD_0
	v_mad_i64_i32 v[50:51], s[20:21], v52, s2, v[50:51]
	v_ashrrev_i32_e32 v57, 31, v56
	v_lshl_add_u64 v[50:51], v[50:51], 0, v[56:57]
	global_load_dwordx2 v[58:59], v[54:55], off offset:16
	s_nop 0
	global_load_dwordx4 v[54:57], v[54:55], off
	v_lshlrev_b32_e32 v130, 6, v60
	global_load_dwordx4 v[148:151], v130, s[44:45] offset:48
	global_load_dwordx4 v[152:155], v130, s[44:45] offset:32
	global_load_dwordx4 v[156:159], v130, s[44:45] offset:16
	global_load_dwordx4 v[166:169], v130, s[44:45]
	global_load_dwordx4 v[170:173], v130, s[44:45] offset:176
	global_load_dwordx4 v[174:177], v130, s[44:45] offset:160
	global_load_dwordx4 v[180:183], v130, s[44:45] offset:144
	global_load_dwordx4 v[198:201], v130, s[44:45] offset:128
	global_load_dwordx4 v[202:205], v130, s[44:45] offset:272
	global_load_dwordx4 v[210:213], v130, s[44:45] offset:304
	global_load_dwordx4 v[214:217], v130, s[44:45] offset:288
	global_load_dwordx4 v[228:231], v130, s[44:45] offset:256
	v_lshl_add_u64 v[50:51], v[50:51], 0, v[178:179]
	s_waitcnt vmcnt(12)
	v_add_f32_e32 v53, v54, v55
	v_mul_f32_e32 v54, v35, v35
	v_mul_f32_e32 v55, v19, v19
	v_fmac_f32_e32 v54, v34, v34
	v_fmac_f32_e32 v55, v18, v18
	v_fmac_f32_e32 v54, v36, v36
	v_fmac_f32_e32 v55, v20, v20
	v_fmac_f32_e32 v54, v37, v37
	v_fmac_f32_e32 v55, v21, v21
	v_fmac_f32_e32 v54, v38, v38
	v_fmac_f32_e32 v55, v22, v22
	v_fmac_f32_e32 v54, v39, v39
	v_fmac_f32_e32 v55, v23, v23
	v_fmac_f32_e32 v54, v40, v40
	v_fmac_f32_e32 v55, v24, v24
	v_add_f32_e32 v53, v53, v56
	v_fmac_f32_e32 v54, v41, v41
	v_fmac_f32_e32 v55, v25, v25
	v_add_f32_e32 v53, v53, v57
	v_fmac_f32_e32 v54, v42, v42
	v_fmac_f32_e32 v55, v26, v26
	v_mul_f32_e32 v57, v3, v3
	v_fmac_f32_e32 v54, v43, v43
	v_fmac_f32_e32 v55, v27, v27
	v_fmac_f32_e32 v57, v2, v2
	v_fmac_f32_e32 v54, v44, v44
	v_fmac_f32_e32 v55, v28, v28
	v_fmac_f32_e32 v57, v4, v4
	v_fmac_f32_e32 v54, v45, v45
	v_fmac_f32_e32 v55, v29, v29
	v_fmac_f32_e32 v57, v5, v5
	v_fmac_f32_e32 v54, v46, v46
	v_fmac_f32_e32 v55, v30, v30
	v_fmac_f32_e32 v57, v6, v6
	v_add_f32_e32 v53, v53, v58
	v_fmac_f32_e32 v54, v47, v47
	v_fmac_f32_e32 v55, v31, v31
	v_fmac_f32_e32 v57, v7, v7
	v_add_f32_e32 v53, v53, v59
	v_fmac_f32_e32 v54, v48, v48
	v_fmac_f32_e32 v55, v32, v32
	v_fmac_f32_e32 v57, v8, v8
	v_fmamk_f32 v53, v53, 0x3b2aaaab, v0
	v_fmac_f32_e32 v54, v49, v49
	v_fmac_f32_e32 v55, v33, v33
	v_fmac_f32_e32 v57, v9, v9
	v_rsq_f32_e32 v53, v53
	v_add_f32_e32 v54, v54, v55
	v_fmac_f32_e32 v57, v10, v10
	v_mov_b32_e32 v55, v54
	v_fmac_f32_e32 v57, v11, v11
	s_nop 1
	v_permlane32_swap_b32 v54, v55
	s_nop 1
	v_fmac_f32_e32 v57, v12, v12
	v_add_f32_e32 v54, v54, v55
	v_fmac_f32_e32 v57, v13, v13
	v_mul_f32_e32 v54, v54, v53
	v_fmac_f32_e32 v57, v14, v14
	v_mul_f32_e32 v56, v53, v54
	v_fmac_f32_e32 v57, v15, v15
	v_pk_mul_f32 v[54:55], v[16:17], v[16:17]
	s_nop 0
	v_add_f32_e32 v54, v54, v57
	v_add_f32_e32 v54, v55, v54
	v_mov_b32_e32 v55, v54
	s_nop 1
	v_permlane32_swap_b32 v54, v55
	s_nop 1
	s_nop 0
	v_add_f32_e32 v54, v54, v55
	v_fmamk_f32 v55, v56, 0x3c800000, v0
	v_rsq_f32_e32 v55, v55
	v_mul_f32_e32 v54, v53, v54
	v_mul_f32_e32 v54, v53, v54
	v_fmamk_f32 v54, v54, 0x3d000000, v0
	v_mul_f32_e32 v61, v53, v55
	v_lshlrev_b32_e32 v55, 6, v60
	v_mul_f32_e32 v34, v34, v61
	v_mul_f32_e32 v35, v35, v61
	v_mul_f32_e32 v46, v46, v61
	v_mul_f32_e32 v36, v36, v61
	v_mul_f32_e32 v37, v37, v61
	v_mul_f32_e32 v38, v38, v61
	v_mul_f32_e32 v39, v39, v61
	v_mul_f32_e32 v42, v42, v61
	v_mul_f32_e32 v43, v43, v61
	v_mul_f32_e32 v47, v47, v61
	v_mul_f32_e32 v40, v40, v61
	v_mul_f32_e32 v41, v41, v61
	v_mul_f32_e32 v44, v44, v61
	v_mul_f32_e32 v45, v45, v61
	v_mul_f32_e32 v48, v48, v61
	v_mul_f32_e32 v49, v49, v61
	v_mul_f32_e32 v18, v18, v61
	v_mul_f32_e32 v19, v19, v61
	v_mul_f32_e32 v30, v30, v61
	v_mul_f32_e32 v20, v20, v61
	v_mul_f32_e32 v21, v21, v61
	v_mul_f32_e32 v22, v22, v61
	v_mul_f32_e32 v23, v23, v61
	v_mul_f32_e32 v26, v26, v61
	v_mul_f32_e32 v27, v27, v61
	v_mul_f32_e32 v31, v31, v61
	v_mul_f32_e32 v33, v33, v61
	v_mul_f32_e32 v24, v24, v61
	v_mul_f32_e32 v25, v25, v61
	v_mul_f32_e32 v28, v28, v61
	v_mul_f32_e32 v29, v29, v61
	v_mul_f32_e32 v32, v32, v61
	v_rsq_f32_e32 v54, v54
	s_waitcnt vmcnt(11)
; DEV u32x4 pk_fp8x16(const f32x16& v) { return (u32x4){pk_fp8x4(v[0], v[1], v[2], v[3]), pk_fp8x4(v[4], v[5], v[6], v[7]), pk_fp8x4(v[8], v[9], v[10], v[11]), pk_fp8x4(v[12], v[13], v[14], v[15])}; }
; DEV u32x4 zero_u32x4() { unsigned z = 0u; asm volatile("" : "+v"(z)); return (u32x4){z, z, z, z}; }
;     template <int TM, int TN> DEV void run(const f32x16 (&acc)[TM][TN], int mw, int cb, int r, int h) const {
;     ...
;             for (int tn = 0; tn < 3; ++tn) { f32x16 v; const float rr = (tn < 2 ? r1 : r2);
; #pragma unroll
;                 for (int i = 0; i < 16; ++i) v[i] = acc[tm][tn][i] * rr * gain[tn * 32 + 16 * h + i];
;                 if (tn == 2 && tok < NLAT) { const int pp = h ? (kidx & 63) : (kidx >> 6); const float* cs = (const float*)(ws + WS_ROPE) + pp * 16;
; #pragma unroll
;                     for (int j = 0; j < 8; ++j) { const float c = cs[2 * j], s = cs[2 * j + 1], a = v[j], bb = v[8 + j]; v[j] = a * c - bb * s; v[8 + j] = bb * c + a * s; } }
; #pragma unroll
;                 for (int i = 0; i < 16; ++i) v[i] *= QS * 8.0f;
;                 *(u32x4*)(dst + tn * 32) = pk_fp8x16(v);
;                 if (tn == 2) *(u32x4*)(dst + 96) = zero_u32x4(); }
	v_mul_f32_e32 v46, v46, v148
	s_waitcnt vmcnt(10)
	v_mul_f32_e32 v42, v42, v152
	s_waitcnt vmcnt(9)
	v_mul_f32_e32 v38, v156, v38
	s_waitcnt vmcnt(8)
	v_mul_f32_e32 v34, v166, v34
	v_mul_f32_e32 v35, v167, v35
	v_mul_f32_e32 v56, 0x3f96c740, v34
	v_mul_f32_e32 v35, 0x3f96c740, v35
	v_mov_b32_e32 v34, v179
	v_cvt_pk_fp8_f32 v34, v56, v35
	v_mul_f32_e32 v36, v168, v36
	v_mul_f32_e32 v37, v169, v37
	v_mul_f32_e32 v39, v157, v39
	v_mul_f32_e32 v43, v43, v153
	v_mul_f32_e32 v47, v47, v149
	v_mul_f32_e32 v36, 0x3f96c740, v36
	v_mul_f32_e32 v37, 0x3f96c740, v37
	v_mul_f32_e32 v38, 0x3f96c740, v38
	v_mul_f32_e32 v39, 0x3f96c740, v39
	v_mul_f32_e32 v42, 0x3f96c740, v42
	v_mul_f32_e32 v43, 0x3f96c740, v43
	v_mul_f32_e32 v46, 0x3f96c740, v46
	v_mul_f32_e32 v47, 0x3f96c740, v47
	v_cvt_pk_fp8_f32 v34, v36, v37 op_sel:[0,0,1]
	v_mov_b32_e32 v35, v179
	v_mov_b32_e32 v36, v179
	v_mov_b32_e32 v37, v179
	v_cvt_pk_fp8_f32 v35, v38, v39
	v_cvt_pk_fp8_f32 v36, v42, v43
	v_cvt_pk_fp8_f32 v37, v46, v47
	v_mul_f32_e32 v40, v158, v40
	v_mul_f32_e32 v41, v159, v41
	v_mul_f32_e32 v44, v44, v154
	v_mul_f32_e32 v45, v45, v155
	v_mul_f32_e32 v48, v48, v150
	v_mul_f32_e32 v49, v49, v151
	v_mul_f32_e32 v40, 0x3f96c740, v40
	v_mul_f32_e32 v41, 0x3f96c740, v41
	v_mul_f32_e32 v44, 0x3f96c740, v44
	v_mul_f32_e32 v45, 0x3f96c740, v45
	v_mul_f32_e32 v48, 0x3f96c740, v48
	v_mul_f32_e32 v49, 0x3f96c740, v49
	v_cvt_pk_fp8_f32 v35, v40, v41 op_sel:[0,0,1]
	v_cvt_pk_fp8_f32 v36, v44, v45 op_sel:[0,0,1]
	v_cvt_pk_fp8_f32 v37, v48, v49 op_sel:[0,0,1]
	global_store_dwordx4 v[50:51], v[34:37], off
	s_nop 0
	s_waitcnt vmcnt(8)
	v_mul_f32_e32 v30, v30, v170
	s_waitcnt vmcnt(7)
	v_mul_f32_e32 v26, v26, v174
	s_waitcnt vmcnt(6)
	v_mul_f32_e32 v22, v22, v180
	s_waitcnt vmcnt(5)
	v_mul_f32_e32 v18, v18, v198
	v_mul_f32_e32 v19, v19, v199
	v_mul_f32_e32 v34, 0x3f96c740, v18
	v_mul_f32_e32 v19, 0x3f96c740, v19
	v_mov_b32_e32 v18, v179
	v_cvt_pk_fp8_f32 v18, v34, v19
	v_mul_f32_e32 v20, v20, v200
	v_mul_f32_e32 v21, v21, v201
	v_mul_f32_e32 v23, v23, v181
	v_mul_f32_e32 v27, v27, v175
	v_mul_f32_e32 v31, v31, v171
	v_mul_f32_e32 v20, 0x3f96c740, v20
	v_mul_f32_e32 v21, 0x3f96c740, v21
	v_mul_f32_e32 v22, 0x3f96c740, v22
	v_mul_f32_e32 v23, 0x3f96c740, v23
	v_mul_f32_e32 v26, 0x3f96c740, v26
	v_mul_f32_e32 v27, 0x3f96c740, v27
	v_mul_f32_e32 v30, 0x3f96c740, v30
	v_mul_f32_e32 v31, 0x3f96c740, v31
	v_cvt_pk_fp8_f32 v18, v20, v21 op_sel:[0,0,1]
	v_mov_b32_e32 v19, v179
	v_mov_b32_e32 v20, v179
	v_mov_b32_e32 v21, v179
	v_cvt_pk_fp8_f32 v19, v22, v23
	v_cvt_pk_fp8_f32 v20, v26, v27
	v_cvt_pk_fp8_f32 v21, v30, v31
	v_mul_f32_e32 v33, v33, v173
	v_mul_f32_e32 v24, v24, v182
	v_mul_f32_e32 v25, v25, v183
	v_mul_f32_e32 v28, v28, v176
	v_mul_f32_e32 v29, v29, v177
	v_mul_f32_e32 v32, v32, v172
	v_mul_f32_e32 v24, 0x3f96c740, v24
	v_mul_f32_e32 v25, 0x3f96c740, v25
	v_mul_f32_e32 v28, 0x3f96c740, v28
	v_mul_f32_e32 v29, 0x3f96c740, v29
	v_mul_f32_e32 v32, 0x3f96c740, v32
	v_mul_f32_e32 v33, 0x3f96c740, v33
	v_cvt_pk_fp8_f32 v19, v24, v25 op_sel:[0,0,1]
	v_cvt_pk_fp8_f32 v20, v28, v29 op_sel:[0,0,1]
	v_cvt_pk_fp8_f32 v21, v32, v33 op_sel:[0,0,1]
	v_mul_f32_e32 v36, v53, v54
	v_mul_f32_e32 v8, v8, v36
	v_pk_mul_f32 v[2:3], v[2:3], v[36:37] op_sel_hi:[1,0]
	global_store_dwordx4 v[50:51], v[18:21], off offset:32
	s_nop 0
	v_pk_mul_f32 v[4:5], v[4:5], v[36:37] op_sel_hi:[1,0]
	v_pk_mul_f32 v[6:7], v[6:7], v[36:37] op_sel_hi:[1,0]
	s_waitcnt vmcnt(5)
	v_mul_f32_e32 v18, v8, v204
	v_mul_f32_e32 v8, v16, v36
	v_pk_mul_f32 v[24:25], v[6:7], v[202:203]
	s_waitcnt vmcnt(2)
	v_pk_mul_f32 v[20:21], v[2:3], v[228:229]
	v_pk_mul_f32 v[2:3], v[10:11], v[36:37] op_sel_hi:[1,0]
	v_mul_f32_e32 v10, v8, v212
	v_mov_b32_e32 v8, v17
	v_pk_mul_f32 v[22:23], v[4:5], v[230:231]
	v_pk_mul_f32 v[4:5], v[12:13], v[36:37] op_sel_hi:[1,0]
	v_pk_mul_f32 v[6:7], v[14:15], v[36:37] op_sel_hi:[1,0]
	v_pk_mul_f32 v[8:9], v[8:9], v[36:37] op_sel_hi:[1,0]
	v_mov_b32_e32 v26, v213
	v_mov_b32_e32 v27, v205
	v_pk_mul_f32 v[2:3], v[2:3], v[214:215]
	v_pk_mul_f32 v[4:5], v[4:5], v[216:217]
	v_pk_mul_f32 v[6:7], v[6:7], v[210:211]
	v_pk_mul_f32 v[8:9], v[8:9], v[26:27]
	s_and_saveexec_b64 s[42:43], vcc
	s_cbranch_execz .LBB0_555
	v_cmp_eq_u32_e32 vcc, 0, v60
	v_bfe_u32 v11, v52, 6, 8
	v_and_b32_e32 v12, 63, v52
	v_cndmask_b32_e32 v11, v12, v11, vcc
	v_lshlrev_b32_e32 v11, 6, v11
	global_load_dwordx4 v[26:29], v11, s[62:63] offset:32
	global_load_dwordx4 v[14:17], v11, s[62:63] offset:16
	global_load_dwordx4 v[30:33], v11, s[62:63]
	global_load_dwordx4 v[34:37], v11, s[62:63] offset:48
	v_mov_b32_e32 v11, v8
	v_mov_b32_e32 v19, v9
	s_waitcnt vmcnt(1)
	v_mov_b32_e32 v39, v32
	v_mov_b32_e32 v32, v31
	v_mov_b32_e32 v38, v30
	v_pk_mul_f32 v[12:13], v[2:3], v[32:33]
	s_waitcnt vmcnt(0)
	v_pk_mul_f32 v[8:9], v[8:9], v[36:37]
	v_pk_fma_f32 v[12:13], v[20:21], v[38:39], v[12:13] neg_lo:[0,0,1] neg_hi:[0,0,1]
	v_pk_mul_f32 v[20:21], v[20:21], v[32:33]
	s_nop 0
	v_pk_fma_f32 v[2:3], v[2:3], v[38:39], v[20:21]
	v_mov_b32_e32 v21, v16
	v_mov_b32_e32 v16, v15
	v_mov_b32_e32 v20, v14
	v_pk_mul_f32 v[14:15], v[4:5], v[16:17]
	v_pk_mul_f32 v[16:17], v[22:23], v[16:17]
	v_pk_fma_f32 v[14:15], v[22:23], v[20:21], v[14:15] neg_lo:[0,0,1] neg_hi:[0,0,1]
	v_pk_fma_f32 v[4:5], v[4:5], v[20:21], v[16:17]
	v_mov_b32_e32 v17, v28
	v_mov_b32_e32 v28, v27
	v_mov_b32_e32 v16, v26
	v_pk_mul_f32 v[20:21], v[6:7], v[28:29]
	v_mov_b32_e32 v22, v14
	v_pk_fma_f32 v[26:27], v[24:25], v[16:17], v[20:21] neg_lo:[0,0,1] neg_hi:[0,0,1]
	v_pk_mul_f32 v[20:21], v[24:25], v[28:29]
	v_mov_b32_e32 v23, v15
	v_pk_fma_f32 v[6:7], v[6:7], v[16:17], v[20:21]
	v_mov_b32_e32 v20, v35
	v_mov_b32_e32 v21, v37
	v_mov_b32_e32 v16, v34
	v_mov_b32_e32 v17, v36
	v_pk_mul_f32 v[20:21], v[10:11], v[20:21]
	v_mul_f32_e32 v10, v10, v34
	v_pk_fma_f32 v[16:17], v[18:19], v[16:17], v[20:21] neg_lo:[0,0,1] neg_hi:[0,0,1]
	v_mul_f32_e32 v18, v18, v35
	v_mov_b32_e32 v11, v8
	v_mov_b32_e32 v19, v9
	v_pk_add_f32 v[10:11], v[10:11], v[18:19]
	v_mov_b32_e32 v20, v12
	v_mov_b32_e32 v21, v13
	v_mov_b32_e32 v24, v26
	v_mov_b32_e32 v25, v27
	v_mov_b32_e32 v18, v16
	v_mov_b32_e32 v9, v17
	v_mov_b32_e32 v8, v11
	s_branch .LBB0_555
